# adds: GLA unit QK^T stage reads the q fragments of each 32-row block from LDS up front into free quads (counted lgkmcnt) instead of one read + lgkmcnt(0) per MFMA
# speedup vs baseline: 1.0003x; 1.0003x over previous
.LBB0_287:
	s_or_b64 exec, exec, s[14:15]
	s_waitcnt lgkmcnt(0)
	s_barrier
	v_readlane_b32 s11, v254, 45
	ds_read_b128 v[6:9], v129
	s_add_u32 s14, s11, s19
	v_readlane_b32 s11, v254, 46
	s_addc_u32 s15, s11, 0
	v_lshl_add_u64 v[2:3], s[14:15], 0, v[2:3]
	v_lshl_add_u64 v[2:3], v[2:3], 0, v[34:35]
	s_waitcnt lgkmcnt(0)
	global_store_dwordx4 v[2:3], v[6:9], off
	ds_read_b128 v[6:9], v130
	v_lshl_add_u64 v[2:3], s[14:15], 0, v[4:5]
	v_lshl_add_u64 v[2:3], v[2:3], 0, v[34:35]
	v_add_u32_e32 v63, v131, v133
	v_readlane_b32 s14, v255, 4
	s_waitcnt lgkmcnt(0)
	global_store_dwordx4 v[2:3], v[6:9], off
	ds_read_b128 v[2:5], v63 offset:17408
	ds_read_b128 v[18:21], v63 offset:17440
	ds_read_b128 v[22:25], v132
	ds_read_b128 v[26:29], v132 offset:32
	ds_read_b128 v[198:201], v63 offset:17472
	ds_read_b128 v[30:33], v132 offset:64
	ds_read_b128 v[202:205], v63 offset:17504
	ds_read_b128 v[66:69], v132 offset:96
	ds_read_b128 v[206:209], v63 offset:17536
	ds_read_b128 v[150:153], v132 offset:128
	ds_read_b128 v[218:221], v63 offset:17568
	ds_read_b128 v[154:157], v132 offset:160
	ds_read_b128 v[222:225], v63 offset:17600
	ds_read_b128 v[158:161], v132 offset:192
	s_waitcnt lgkmcnt(11)
	v_mfma_f32_32x32x16_bf16 v[2:17], v[2:5], v[22:25], 0
	v_readlane_b32 s15, v255, 5
	s_lshl_b32 s11, s18, 8
	s_lshl_b32 s8, s8, 1
	s_waitcnt lgkmcnt(10)
	v_mfma_f32_32x32x16_bf16 v[2:17], v[18:21], v[26:29], v[2:17]
	ds_read_b128 v[226:229], v63 offset:17632
	ds_read_b128 v[162:165], v132 offset:224
	s_waitcnt lgkmcnt(10)
	v_mfma_f32_32x32x16_bf16 v[2:17], v[198:201], v[30:33], v[2:17]
	s_waitcnt lgkmcnt(8)
	v_mfma_f32_32x32x16_bf16 v[2:17], v[202:205], v[66:69], v[2:17]
	s_waitcnt lgkmcnt(6)
	v_mfma_f32_32x32x16_bf16 v[2:17], v[206:209], v[150:153], v[2:17]
	s_waitcnt lgkmcnt(4)
	v_mfma_f32_32x32x16_bf16 v[2:17], v[218:221], v[154:157], v[2:17]
	s_waitcnt lgkmcnt(2)
	v_mfma_f32_32x32x16_bf16 v[2:17], v[222:225], v[158:161], v[2:17]
	s_waitcnt lgkmcnt(0)
	v_mfma_f32_32x32x16_bf16 v[2:17], v[226:229], v[162:165], v[2:17]
	s_nop 11
	v_cndmask_b32_e64 v18, v2, 0, s[14:15]
	v_readlane_b32 s14, v255, 6
	v_readlane_b32 s15, v255, 7
	v_cndmask_b32_e64 v149, v18, v2, s[12:13]
	v_cndmask_b32_e64 v168, 0, v3, s[12:13]
	v_cndmask_b32_e64 v169, v4, 0, s[14:15]
	v_readlane_b32 s14, v255, 8
	v_readlane_b32 s15, v255, 9
	ds_read_b128 v[18:21], v63 offset:26144
	v_cndmask_b32_e64 v172, v7, 0, s[20:21]
	v_cndmask_b32_e64 v170, v5, 0, s[14:15]
	ds_read_b128 v[2:5], v63 offset:26112
	ds_read_b128 v[198:201], v63 offset:26176
	ds_read_b128 v[202:205], v63 offset:26208
	ds_read_b128 v[206:209], v63 offset:26240
	ds_read_b128 v[218:221], v63 offset:26272
	ds_read_b128 v[222:225], v63 offset:26304
	ds_read_b128 v[226:229], v63 offset:26336
	v_readlane_b32 s14, v255, 10
	v_readlane_b32 s15, v255, 11
	v_cndmask_b32_e64 v173, v8, 0, s[22:23]
	v_cndmask_b32_e64 v174, v9, 0, s[24:25]
	v_cndmask_b32_e64 v171, v6, 0, s[14:15]
	v_cndmask_b32_e64 v175, v10, 0, s[26:27]
	v_cndmask_b32_e64 v176, v11, 0, s[28:29]
	v_cndmask_b32_e64 v177, v12, 0, s[30:31]
	v_cndmask_b32_e64 v178, v13, 0, s[34:35]
	v_cndmask_b32_e64 v179, v14, 0, s[2:3]
	v_cndmask_b32_e64 v180, v15, 0, s[38:39]
	v_cndmask_b32_e64 v181, v16, 0, s[40:41]
	v_cndmask_b32_e64 v182, v17, 0, s[42:43]
	s_waitcnt lgkmcnt(6)
	v_mfma_f32_32x32x16_bf16 v[2:17], v[2:5], v[22:25], 0
	v_readlane_b32 s14, v254, 49
	v_cvt_pk_bf16_f32 v22, v175, v176
	v_cvt_pk_bf16_f32 v23, v177, v178
	v_cvt_pk_bf16_f32 v24, v179, v180
	v_cvt_pk_bf16_f32 v25, v181, v182
	v_mfma_f32_32x32x16_bf16 v[2:17], v[18:21], v[26:29], v[2:17]
	s_waitcnt lgkmcnt(5)
	v_mfma_f32_32x32x16_bf16 v[2:17], v[198:201], v[30:33], v[2:17]
	s_waitcnt lgkmcnt(4)
	v_mfma_f32_32x32x16_bf16 v[2:17], v[202:205], v[66:69], v[2:17]
	v_lshl_add_u64 v[68:69], v[40:41], 0, s[8:9]
	v_lshlrev_b64 v[66:67], 15, v[64:65]
	v_lshl_add_u64 v[66:67], v[58:59], 0, v[66:67]
	v_lshlrev_b64 v[64:65], 16, v[64:65]
	s_waitcnt lgkmcnt(3)
	v_mfma_f32_32x32x16_bf16 v[2:17], v[206:209], v[150:153], v[2:17]
	s_waitcnt lgkmcnt(2)
	v_mfma_f32_32x32x16_bf16 v[2:17], v[218:221], v[154:157], v[2:17]
	s_waitcnt lgkmcnt(1)
	v_mfma_f32_32x32x16_bf16 v[2:17], v[222:225], v[158:161], v[2:17]
	s_waitcnt lgkmcnt(0)
	v_mfma_f32_32x32x16_bf16 v[2:17], v[226:229], v[162:165], v[2:17]
	v_or_b32_e32 v163, s11, v167
	v_cvt_pk_bf16_f32 v19, v169, v170
	v_cvt_pk_bf16_f32 v20, v171, v172
	v_cvt_pk_bf16_f32 v21, v173, v174
	s_nop 7
	v_cndmask_b32_e64 v18, v2, 0, s[44:45]
	v_cndmask_b32_e64 v30, v18, v2, s[46:47]
	v_add_u32_e32 v2, s14, v163
	v_cndmask_b32_e64 v31, 0, v3, s[46:47]
	v_ashrrev_i32_e32 v3, 31, v2
	v_lshlrev_b64 v[2:3], 12, v[2:3]
	v_lshl_add_u64 v[152:153], v[68:69], 0, v[2:3]
	v_cndmask_b32_e64 v32, v4, 0, s[50:51]
	v_cndmask_b32_e64 v33, v5, 0, s[52:53]
	global_load_dwordx2 v[2:3], v[152:153], off
	global_load_dwordx2 v[4:5], v[152:153], off offset:16
	global_load_dwordx2 v[26:27], v[152:153], off offset:32
	global_load_dwordx2 v[28:29], v[152:153], off offset:48
	global_load_dwordx2 v[198:199], v[152:153], off offset:64
	global_load_dwordx2 v[200:201], v[152:153], off offset:80
	global_load_dwordx2 v[202:203], v[152:153], off offset:96
	global_load_dwordx2 v[204:205], v[152:153], off offset:112
	v_readlane_b32 s14, v254, 51
	s_nop 1
	v_add_u32_e32 v212, s14, v163
	v_ashrrev_i32_e32 v213, 31, v212
	v_lshlrev_b64 v[212:213], 12, v[212:213]
	v_lshl_add_u64 v[230:231], v[68:69], 0, v[212:213]
	global_load_dwordx2 v[206:207], v[230:231], off
	global_load_dwordx2 v[208:209], v[230:231], off offset:16
	global_load_dwordx2 v[218:219], v[230:231], off offset:32
	global_load_dwordx2 v[220:221], v[230:231], off offset:48
	global_load_dwordx2 v[222:223], v[230:231], off offset:64
	global_load_dwordx2 v[224:225], v[230:231], off offset:80
	global_load_dwordx2 v[226:227], v[230:231], off offset:96
	global_load_dwordx2 v[228:229], v[230:231], off offset:112
	v_add_u32_e32 v212, s11, v134
	v_ashrrev_i32_e32 v213, 31, v212
	v_lshlrev_b64 v[212:213], 12, v[212:213]
	v_lshl_add_u64 v[232:233], s[6:7], 0, v[212:213]
	v_lshl_add_u64 v[232:233], v[232:233], 0, s[8:9]
	v_mov_b32_e32 v234, v62
	v_mov_b32_e32 v235, v35
	v_lshl_add_u64 v[232:233], v[232:233], 0, v[234:235]
	global_load_dwordx4 v[238:241], v[232:233], off
	global_load_dwordx4 v[242:245], v[232:233], off offset:32
	global_load_dwordx4 v[246:249], v[232:233], off offset:64
	global_load_dwordx4 v[250:253], v[232:233], off offset:96
	v_cvt_pk_bf16_f32 v18, v149, v168
	v_cndmask_b32_e64 v63, v6, 0, s[54:55]
	v_cndmask_b32_e64 v150, v7, 0, s[78:79]
	v_cndmask_b32_e64 v151, v8, 0, s[96:97]
	v_cndmask_b32_e64 v154, v9, 0, s[0:1]
	v_cndmask_b32_e64 v155, v10, 0, s[76:77]
	v_cndmask_b32_e64 v156, v11, 0, s[4:5]
	v_cndmask_b32_e64 v157, v12, 0, s[64:65]
	v_cndmask_b32_e64 v158, v13, 0, s[66:67]
	v_cndmask_b32_e64 v159, v14, 0, s[68:69]
	v_cndmask_b32_e64 v160, v15, 0, s[70:71]
	v_cndmask_b32_e64 v161, v16, 0, s[72:73]
	v_cndmask_b32_e64 v162, v17, 0, s[74:75]
	s_waitcnt vmcnt(18)
	v_mfma_f32_32x32x16_bf16 v[2:17], v[2:5], v[18:21], 0
	s_waitcnt vmcnt(16)
	v_mfma_f32_32x32x16_bf16 v[2:17], v[26:29], v[22:25], v[2:17]
	v_cvt_pk_bf16_f32 v26, v30, v31
	v_cvt_pk_bf16_f32 v27, v32, v33
	v_cvt_pk_bf16_f32 v28, v63, v150
	v_cvt_pk_bf16_f32 v29, v151, v154
	v_mov_b32_e32 v63, v35
	s_waitcnt vmcnt(14)
	v_mfma_f32_32x32x16_bf16 v[2:17], v[198:201], v[26:29], v[2:17]
	v_cvt_pk_bf16_f32 v30, v155, v156
	v_cvt_pk_bf16_f32 v31, v157, v158
	v_cvt_pk_bf16_f32 v32, v159, v160
	v_cvt_pk_bf16_f32 v33, v161, v162
	s_waitcnt vmcnt(12)
	s_nop 0
	v_mfma_f32_32x32x16_bf16 v[2:17], v[202:205], v[30:33], v[2:17]
	s_nop 11
	v_cvt_pk_bf16_f32 v2, v2, v3
	v_cvt_pk_bf16_f32 v3, v4, v5
	v_cvt_pk_bf16_f32 v4, v6, v7
	v_cvt_pk_bf16_f32 v5, v8, v9
	global_store_dwordx4 v[66:67], v[2:5], off
	s_nop 1
	v_cvt_pk_bf16_f32 v2, v10, v11
	v_cvt_pk_bf16_f32 v3, v12, v13
	v_cvt_pk_bf16_f32 v4, v14, v15
	v_cvt_pk_bf16_f32 v5, v16, v17
	global_store_dwordx4 v[66:67], v[2:5], off offset:1024
	s_nop 1
	s_waitcnt vmcnt(12)
	v_mfma_f32_32x32x16_bf16 v[2:17], v[206:209], v[18:21], 0
	s_waitcnt vmcnt(10)
	v_mfma_f32_32x32x16_bf16 v[2:17], v[218:221], v[22:25], v[2:17]
	s_waitcnt vmcnt(8)
	v_mfma_f32_32x32x16_bf16 v[2:17], v[222:225], v[26:29], v[2:17]
	s_waitcnt vmcnt(6)
	v_mfma_f32_32x32x16_bf16 v[2:17], v[226:229], v[30:33], v[2:17]
	s_nop 11
	v_cvt_pk_bf16_f32 v2, v2, v3
	v_cvt_pk_bf16_f32 v3, v4, v5
	v_cvt_pk_bf16_f32 v4, v6, v7
	v_cvt_pk_bf16_f32 v5, v8, v9
	global_store_dwordx4 v[66:67], v[2:5], off offset:2048
	s_nop 1
	v_cvt_pk_bf16_f32 v2, v10, v11
	v_cvt_pk_bf16_f32 v3, v12, v13
	v_cvt_pk_bf16_f32 v4, v14, v15
	v_cvt_pk_bf16_f32 v5, v16, v17
	global_store_dwordx4 v[66:67], v[2:5], off offset:3072
	s_nop 1
	v_add_u32_e32 v63, v131, v137
	ds_read_b128 v[2:5], v63 offset:34816
	ds_read_b128 v[66:69], v63 offset:34848
	v_readlane_b32 s8, v254, 53
	s_waitcnt vmcnt(7) lgkmcnt(1)
	v_mfma_f32_32x32x16_bf16 v[2:17], v[238:241], v[2:5], 0
	s_waitcnt vmcnt(6) lgkmcnt(0)
	v_mfma_f32_32x32x16_bf16 v[2:17], v[242:245], v[66:69], v[2:17]
	ds_read_b128 v[66:69], v63 offset:34880
	s_waitcnt vmcnt(5) lgkmcnt(0)
	v_mfma_f32_32x32x16_bf16 v[2:17], v[246:249], v[66:69], v[2:17]
	ds_read_b128 v[66:69], v63 offset:34912
	s_waitcnt vmcnt(4) lgkmcnt(0)
	v_mfma_f32_32x32x16_bf16 v[2:17], v[250:253], v[66:69], v[2:17]
	v_add_u32_e32 v66, s8, v135
	v_readlane_b32 s8, v254, 54
	s_nop 1
	v_add_u32_e32 v67, s8, v135
	v_readlane_b32 s8, v254, 55
	s_nop 5
	v_cvt_pk_bf16_f32 v2, v2, s0
	ds_write_b16 v136, v2 offset:59392
	v_cvt_pk_bf16_f32 v2, v3, s0
	ds_write_b16 v136, v2 offset:59648
	v_cvt_pk_bf16_f32 v2, v4, s0
	ds_write_b16 v136, v2 offset:59904
	v_cvt_pk_bf16_f32 v2, v5, s0
	ds_write_b16 v136, v2 offset:60160
	v_cvt_pk_bf16_f32 v2, v6, s0
	ds_write_b16 v136, v2 offset:61440
	v_cvt_pk_bf16_f32 v2, v7, s0
	ds_write_b16 v136, v2 offset:61696
	v_cvt_pk_bf16_f32 v2, v8, s0
	ds_write_b16 v136, v2 offset:61952
	v_cvt_pk_bf16_f32 v2, v9, s0
	ds_write_b16 v136, v2 offset:62208
	v_cvt_pk_bf16_f32 v2, v10, s0
	ds_write_b16 v136, v2 offset:63488
	v_cvt_pk_bf16_f32 v2, v11, s0
	ds_write_b16 v136, v2 offset:63744
	v_cvt_pk_bf16_f32 v2, v12, s0
	ds_write_b16 v136, v2 offset:64000
	v_cvt_pk_bf16_f32 v2, v13, s0
	ds_write_b16 v136, v2 offset:64256
	v_cvt_pk_bf16_f32 v2, v14, s0
	ds_write_b16 v66, v2 offset:59392
	v_cvt_pk_bf16_f32 v2, v15, s0
	ds_write_b16 v67, v2 offset:59392
	v_cvt_pk_bf16_f32 v2, v16, s0
	v_add_u32_e32 v68, s8, v135
	v_readlane_b32 s8, v254, 57
	ds_write_b16 v68, v2 offset:59392
	v_cvt_pk_bf16_f32 v2, v17, s0
	v_add_u32_e32 v69, s8, v135
	ds_write_b16 v69, v2 offset:59392
	ds_read_b128 v[2:5], v63 offset:39424
	ds_read_b128 v[150:153], v63 offset:39456
	s_waitcnt lgkmcnt(1)
	v_mfma_f32_32x32x16_bf16 v[2:17], v[238:241], v[2:5], 0
	v_readlane_b32 s8, v254, 36
	s_add_i32 s10, s10, s8
	v_readlane_b32 s8, v255, 12
	s_add_i32 s16, s16, s8
	v_readlane_b32 s8, v255, 13
	s_add_i32 s17, s17, s8
	s_cmpk_gt_i32 s10, 0x1ff
	s_waitcnt lgkmcnt(0)
	v_mfma_f32_32x32x16_bf16 v[2:17], v[242:245], v[150:153], v[2:17]
	ds_read_b128 v[150:153], v63 offset:39488
	s_waitcnt lgkmcnt(0)
	v_mfma_f32_32x32x16_bf16 v[2:17], v[246:249], v[150:153], v[2:17]
	ds_read_b128 v[150:153], v63 offset:39520
	s_waitcnt lgkmcnt(0)
	v_mfma_f32_32x32x16_bf16 v[2:17], v[250:253], v[150:153], v[2:17]
	s_nop 11
	v_cvt_pk_bf16_f32 v2, v2, s0
	ds_write_b16 v136, v2 offset:59456
	v_cvt_pk_bf16_f32 v2, v3, s0
	ds_write_b16 v136, v2 offset:59712
	v_cvt_pk_bf16_f32 v2, v4, s0
	ds_write_b16 v136, v2 offset:59968
	v_cvt_pk_bf16_f32 v2, v5, s0
	ds_write_b16 v136, v2 offset:60224
	v_cvt_pk_bf16_f32 v2, v6, s0
	ds_write_b16 v136, v2 offset:61504
	v_cvt_pk_bf16_f32 v2, v7, s0
	ds_write_b16 v136, v2 offset:61760
	v_cvt_pk_bf16_f32 v2, v8, s0
	ds_write_b16 v136, v2 offset:62016
	v_cvt_pk_bf16_f32 v2, v9, s0
	ds_write_b16 v136, v2 offset:62272
	v_cvt_pk_bf16_f32 v2, v10, s0
	ds_write_b16 v136, v2 offset:63552
	v_cvt_pk_bf16_f32 v2, v11, s0
	ds_write_b16 v136, v2 offset:63808
	v_cvt_pk_bf16_f32 v2, v12, s0
	ds_write_b16 v136, v2 offset:64064
	v_cvt_pk_bf16_f32 v2, v13, s0
	ds_write_b16 v136, v2 offset:64320
	v_cvt_pk_bf16_f32 v2, v14, s0
	ds_write_b16 v66, v2 offset:59456
	v_cvt_pk_bf16_f32 v2, v15, s0
	ds_write_b16 v67, v2 offset:59456
	v_cvt_pk_bf16_f32 v2, v16, s0
	ds_write_b16 v68, v2 offset:59456
	v_cvt_pk_bf16_f32 v2, v17, s0
	ds_write_b16 v69, v2 offset:59456
	ds_read_b128 v[2:5], v63 offset:44032
	ds_read_b128 v[150:153], v63 offset:44064
	s_waitcnt lgkmcnt(1)
	v_mfma_f32_32x32x16_bf16 v[2:17], v[238:241], v[2:5], 0
	s_waitcnt lgkmcnt(0)
	v_mfma_f32_32x32x16_bf16 v[2:17], v[242:245], v[150:153], v[2:17]
	ds_read_b128 v[150:153], v63 offset:44096
	s_waitcnt lgkmcnt(0)
	v_mfma_f32_32x32x16_bf16 v[2:17], v[246:249], v[150:153], v[2:17]
	ds_read_b128 v[150:153], v63 offset:44128
	s_waitcnt lgkmcnt(0)
	v_mfma_f32_32x32x16_bf16 v[2:17], v[250:253], v[150:153], v[2:17]
	s_nop 11
	v_cvt_pk_bf16_f32 v2, v2, s0
	ds_write_b16 v136, v2 offset:59520
	v_cvt_pk_bf16_f32 v2, v3, s0
	ds_write_b16 v136, v2 offset:59776
	v_cvt_pk_bf16_f32 v2, v4, s0
	ds_write_b16 v136, v2 offset:60032
	v_cvt_pk_bf16_f32 v2, v5, s0
	ds_write_b16 v136, v2 offset:60288
	v_cvt_pk_bf16_f32 v2, v6, s0
	ds_write_b16 v136, v2 offset:61568
	v_cvt_pk_bf16_f32 v2, v7, s0
	ds_write_b16 v136, v2 offset:61824
	v_cvt_pk_bf16_f32 v2, v8, s0
	ds_write_b16 v136, v2 offset:62080
	v_cvt_pk_bf16_f32 v2, v9, s0
	ds_write_b16 v136, v2 offset:62336
	v_cvt_pk_bf16_f32 v2, v10, s0
	ds_write_b16 v136, v2 offset:63616
	v_cvt_pk_bf16_f32 v2, v11, s0
	ds_write_b16 v136, v2 offset:63872
	v_cvt_pk_bf16_f32 v2, v12, s0
	ds_write_b16 v136, v2 offset:64128
	v_cvt_pk_bf16_f32 v2, v13, s0
	ds_write_b16 v136, v2 offset:64384
	v_cvt_pk_bf16_f32 v2, v14, s0
	ds_write_b16 v66, v2 offset:59520
	v_cvt_pk_bf16_f32 v2, v15, s0
	ds_write_b16 v67, v2 offset:59520
	v_cvt_pk_bf16_f32 v2, v16, s0
	ds_write_b16 v68, v2 offset:59520
	v_cvt_pk_bf16_f32 v2, v17, s0
	ds_write_b16 v69, v2 offset:59520
	ds_read_b128 v[2:5], v63 offset:48640
	ds_read_b128 v[150:153], v63 offset:48672
	s_waitcnt lgkmcnt(1)
	v_mfma_f32_32x32x16_bf16 v[2:17], v[238:241], v[2:5], 0
	ds_read_b128 v[26:29], v63 offset:48704
	s_waitcnt lgkmcnt(1)
	v_mfma_f32_32x32x16_bf16 v[2:17], v[242:245], v[150:153], v[2:17]
	s_waitcnt lgkmcnt(0)
	v_mfma_f32_32x32x16_bf16 v[2:17], v[246:249], v[26:29], v[2:17]
	ds_read_b128 v[22:25], v63 offset:48736
	s_waitcnt lgkmcnt(0)
	v_mfma_f32_32x32x16_bf16 v[2:17], v[250:253], v[22:25], v[2:17]
	s_nop 11
	v_cvt_pk_bf16_f32 v2, v2, s0
	ds_write_b16 v136, v2 offset:59584
	v_cvt_pk_bf16_f32 v2, v3, s0
	ds_write_b16 v136, v2 offset:59840
	v_cvt_pk_bf16_f32 v2, v4, s0
	ds_write_b16 v136, v2 offset:60096
	v_cvt_pk_bf16_f32 v2, v5, s0
	ds_write_b16 v136, v2 offset:60352
	v_cvt_pk_bf16_f32 v2, v6, s0
	ds_write_b16 v136, v2 offset:61632
	v_cvt_pk_bf16_f32 v2, v7, s0
	ds_write_b16 v136, v2 offset:61888
	v_cvt_pk_bf16_f32 v2, v8, s0
	ds_write_b16 v136, v2 offset:62144
	v_cvt_pk_bf16_f32 v2, v9, s0
	ds_write_b16 v136, v2 offset:62400
	v_cvt_pk_bf16_f32 v2, v10, s0
	ds_write_b16 v136, v2 offset:63680
	v_cvt_pk_bf16_f32 v2, v11, s0
	ds_write_b16 v136, v2 offset:63936
	v_cvt_pk_bf16_f32 v2, v12, s0
	ds_write_b16 v136, v2 offset:64192
	v_cvt_pk_bf16_f32 v2, v13, s0
	ds_write_b16 v136, v2 offset:64448
	v_cvt_pk_bf16_f32 v2, v14, s0
	ds_write_b16 v66, v2 offset:59584
	v_cvt_pk_bf16_f32 v2, v15, s0
	ds_write_b16 v67, v2 offset:59584
	v_cvt_pk_bf16_f32 v2, v16, s0
	ds_write_b16 v68, v2 offset:59584
	v_cvt_pk_bf16_f32 v2, v17, s0
	ds_write_b16 v69, v2 offset:59584
	s_waitcnt lgkmcnt(0)
	v_add_u32_e32 v4, v70, v138
	ds_read_b128 v[198:201], v4 offset:59392
	v_add_u32_e32 v4, v70, v139
	ds_read_b128 v[202:205], v4 offset:59392
	v_add_u32_e32 v4, v70, v140
	ds_read_b128 v[206:209], v4 offset:59392
	v_add_u32_e32 v4, v70, v141
	ds_read_b128 v[218:221], v4 offset:59392
	v_add_u32_e32 v4, v70, v143
	ds_read_b128 v[222:225], v4 offset:59392
	v_add_u32_e32 v4, v70, v144
	ds_read_b128 v[226:229], v4 offset:59392
	v_add_u32_e32 v4, v70, v145
	ds_read_b128 v[230:233], v4 offset:59392
	v_add_u32_e32 v4, v70, v146
	ds_read_b128 v[238:241], v4 offset:59392
	v_lshl_add_u64 v[2:3], v[38:39], 0, v[64:65]
	v_lshl_add_u64 v[8:9], v[2:3], 0, v[42:43]
	s_waitcnt lgkmcnt(7)
	global_store_dwordx4 v[8:9], v[198:201], off
	v_lshl_add_u64 v[8:9], v[2:3], 0, v[44:45]
	s_waitcnt lgkmcnt(6)
	global_store_dwordx4 v[8:9], v[202:205], off
	v_lshl_add_u64 v[8:9], v[2:3], 0, v[46:47]
	s_waitcnt lgkmcnt(5)
	global_store_dwordx4 v[8:9], v[206:209], off
	v_lshl_add_u64 v[8:9], v[2:3], 0, v[48:49]
	s_waitcnt lgkmcnt(4)
	global_store_dwordx4 v[8:9], v[218:221], off
	v_lshl_add_u64 v[8:9], v[2:3], 0, v[50:51]
	s_waitcnt lgkmcnt(3)
	global_store_dwordx4 v[8:9], v[222:225], off
	v_lshl_add_u64 v[8:9], v[2:3], 0, v[52:53]
	s_waitcnt lgkmcnt(2)
	global_store_dwordx4 v[8:9], v[226:229], off
	v_lshl_add_u64 v[8:9], v[2:3], 0, v[54:55]
	s_waitcnt lgkmcnt(1)
	global_store_dwordx4 v[8:9], v[230:233], off
	v_lshl_add_u64 v[2:3], v[2:3], 0, v[56:57]
	s_waitcnt lgkmcnt(0)
	global_store_dwordx4 v[2:3], v[238:241], off
	s_barrier
	s_cbranch_scc1 .LBB0_294
